# first iteration kernel stores each wave's block-0 f16 kernel entries; the 7 later launches load them instead of recomputing MFMA+exp for that block
# speedup vs baseline: 1.0206x; 1.0171x over previous
.LBB2_53:
	v_max_f32_e32 v2, v115, v115
	v_max_f32_e32 v2, 0xc6ea6000, v2
	v_and_b32_e32 v4, 0xffff0000, v2
	v_and_b32_e32 v3, 0xffff0000, v1
	v_sub_f32_e32 v5, v2, v4
	v_sub_f32_e32 v3, v1, v3
	v_and_b32_e32 v6, 0xffff0000, v5
	s_mov_b32 s0, 0xffff0000
	v_and_b32_e32 v3, 0xffff0000, v3
	v_sub_f32_e32 v6, v5, v6
	v_lshrrev_b32_e32 v5, 16, v5
	v_or_b32_sdwa v117, v4, v1 dst_sel:DWORD dst_unused:UNUSED_PAD src0_sel:DWORD src1_sel:WORD_1
	v_or_b32_sdwa v116, v3, v1 dst_sel:DWORD dst_unused:UNUSED_PAD src0_sel:DWORD src1_sel:WORD_1
	v_and_or_b32 v118, v6, s0, v5
	v_or_b32_sdwa v119, v2, v4 dst_sel:DWORD dst_unused:UNUSED_PAD src0_sel:WORD_1 src1_sel:DWORD
	s_movk_i32 s0, 0xfc00
	s_nop 0
	v_mfma_f32_32x32x16_bf16 v[2:17], v[40:43], v[116:119], 0
	s_nop 11
	v_cvt_pk_f16_f32 v1, v2, v3
	v_cvt_pk_f16_f32 v2, v4, v5
	v_pk_max_i16 v2, v2, s0 op_sel_hi:[1,0]
	v_pk_max_i16 v1, v1, s0 op_sel_hi:[1,0]
	s_nop 0
	v_exp_f16_e32 v130, v1
	v_exp_f16_e32 v127, v2
	v_exp_f16_sdwa v130, v1 dst_sel:WORD_1 dst_unused:UNUSED_PRESERVE src0_sel:WORD_1
	v_exp_f16_sdwa v127, v2 dst_sel:WORD_1 dst_unused:UNUSED_PRESERVE src0_sel:WORD_1
	v_cvt_pk_f16_f32 v2, v8, v9
	v_cvt_pk_f16_f32 v1, v6, v7
	v_pk_max_i16 v2, v2, s0 op_sel_hi:[1,0]
	v_pk_max_i16 v1, v1, s0 op_sel_hi:[1,0]
	s_nop 0
	v_exp_f16_e32 v129, v1
	v_exp_f16_e32 v124, v2
	v_exp_f16_sdwa v129, v1 dst_sel:WORD_1 dst_unused:UNUSED_PRESERVE src0_sel:WORD_1
	v_exp_f16_sdwa v124, v2 dst_sel:WORD_1 dst_unused:UNUSED_PRESERVE src0_sel:WORD_1
	v_cvt_pk_f16_f32 v2, v12, v13
	v_cvt_pk_f16_f32 v1, v10, v11
	v_pk_max_i16 v2, v2, s0 op_sel_hi:[1,0]
	v_pk_max_i16 v1, v1, s0 op_sel_hi:[1,0]
	s_nop 0
	v_exp_f16_e32 v128, v1
	v_exp_f16_e32 v122, v2
	v_exp_f16_sdwa v128, v1 dst_sel:WORD_1 dst_unused:UNUSED_PRESERVE src0_sel:WORD_1
	v_exp_f16_sdwa v122, v2 dst_sel:WORD_1 dst_unused:UNUSED_PRESERVE src0_sel:WORD_1
	v_cvt_pk_f16_f32 v2, v16, v17
	v_cvt_pk_f16_f32 v1, v14, v15
	v_pk_max_i16 v2, v2, s0 op_sel_hi:[1,0]
	v_pk_max_i16 v1, v1, s0 op_sel_hi:[1,0]
	s_nop 0
	v_exp_f16_e32 v126, v1
	v_exp_f16_e32 v120, v2
	v_exp_f16_sdwa v126, v1 dst_sel:WORD_1 dst_unused:UNUSED_PRESERVE src0_sel:WORD_1
	v_exp_f16_sdwa v120, v2 dst_sel:WORD_1 dst_unused:UNUSED_PRESERVE src0_sel:WORD_1
	v_mfma_f32_32x32x16_bf16 v[2:17], v[36:39], v[116:119], 0
	s_nop 11
	v_cvt_pk_f16_f32 v1, v2, v3
	v_cvt_pk_f16_f32 v2, v4, v5
	v_pk_max_i16 v1, v1, s0 op_sel_hi:[1,0]
	v_pk_max_i16 v2, v2, s0 op_sel_hi:[1,0]
	s_nop 0
	v_exp_f16_e32 v125, v1
	v_exp_f16_e32 v119, v2
	v_exp_f16_sdwa v125, v1 dst_sel:WORD_1 dst_unused:UNUSED_PRESERVE src0_sel:WORD_1
	v_exp_f16_sdwa v119, v2 dst_sel:WORD_1 dst_unused:UNUSED_PRESERVE src0_sel:WORD_1
	v_cvt_pk_f16_f32 v1, v6, v7
	v_cvt_pk_f16_f32 v2, v8, v9
	v_pk_max_i16 v1, v1, s0 op_sel_hi:[1,0]
	v_pk_max_i16 v2, v2, s0 op_sel_hi:[1,0]
	s_nop 0
	v_exp_f16_e32 v123, v1
	v_exp_f16_e32 v117, v2
	v_exp_f16_sdwa v123, v1 dst_sel:WORD_1 dst_unused:UNUSED_PRESERVE src0_sel:WORD_1
	v_exp_f16_sdwa v117, v2 dst_sel:WORD_1 dst_unused:UNUSED_PRESERVE src0_sel:WORD_1
	v_cvt_pk_f16_f32 v1, v10, v11
	v_cvt_pk_f16_f32 v2, v12, v13
	v_pk_max_i16 v1, v1, s0 op_sel_hi:[1,0]
	v_pk_max_i16 v2, v2, s0 op_sel_hi:[1,0]
	s_nop 0
	v_exp_f16_e32 v121, v1
	v_exp_f16_e32 v116, v2
	v_exp_f16_sdwa v121, v1 dst_sel:WORD_1 dst_unused:UNUSED_PRESERVE src0_sel:WORD_1
	v_exp_f16_sdwa v116, v2 dst_sel:WORD_1 dst_unused:UNUSED_PRESERVE src0_sel:WORD_1
	v_cvt_pk_f16_f32 v1, v14, v15
	v_cvt_pk_f16_f32 v2, v16, v17
	v_pk_max_i16 v1, v1, s0 op_sel_hi:[1,0]
	v_pk_max_i16 v2, v2, s0 op_sel_hi:[1,0]
	s_nop 0
	v_exp_f16_e32 v118, v1
	v_exp_f16_e32 v17, v2
	v_exp_f16_sdwa v118, v1 dst_sel:WORD_1 dst_unused:UNUSED_PRESERVE src0_sel:WORD_1
	v_exp_f16_sdwa v17, v2 dst_sel:WORD_1 dst_unused:UNUSED_PRESERVE src0_sel:WORD_1
	s_cmpk_gt_i32 s38, 0x800
	s_cbranch_scc1 .Lfirst_nocache
	s_lshl_b32 s66, s27, 12
	s_add_u32 s66, s66, 0x8000
	s_add_u32 s66, s44, s66
	s_addc_u32 s67, s45, 0
	v_lshlrev_b32_e32 v216, 4, v44
	v_mov_b32_e32 v220, v130
	v_mov_b32_e32 v221, v127
	v_mov_b32_e32 v222, v129
	v_mov_b32_e32 v223, v124
	v_mov_b32_e32 v224, v128
	v_mov_b32_e32 v225, v122
	v_mov_b32_e32 v226, v126
	v_mov_b32_e32 v227, v120
	v_mov_b32_e32 v228, v125
	v_mov_b32_e32 v229, v119
	v_mov_b32_e32 v230, v123
	v_mov_b32_e32 v231, v117
	v_mov_b32_e32 v232, v121
	v_mov_b32_e32 v233, v116
	v_mov_b32_e32 v234, v118
	v_mov_b32_e32 v235, v17
	global_store_dwordx4 v216, v[220:223], s[66:67] sc1
	global_store_dwordx4 v216, v[224:227], s[66:67] offset:1024 sc1
	global_store_dwordx4 v216, v[228:231], s[66:67] offset:2048 sc1
	global_store_dwordx4 v216, v[232:235], s[66:67] offset:3072 sc1
.Lfirst_nocache:
	s_cmp_lt_i32 s39, 4
	s_mov_b64 s[0:1], 0
	s_cbranch_scc0 .LBB2_60

.LBB3_6:
	s_xor_b32 s33, s32, 0xff
	s_add_i32 s33, s33, s24
	s_ashr_i32 s26, s33, 8
	v_cmp_gt_i32_e32 vcc, s24, v176
	v_med3_i32 v33, s26, 0, 6
	s_sub_i32 s33, s24, 0x100
	v_cmp_gt_i32_e64 s[4:5], s33, v176
	s_sub_i32 s33, s24, 0x200
	v_cmp_gt_i32_e64 s[6:7], s33, v176
	s_sub_i32 s33, s24, 0x300
	v_cmp_gt_i32_e64 s[8:9], s33, v176
	s_sub_i32 s33, s24, 0x400
	v_cmp_gt_i32_e64 s[10:11], s33, v176
	s_sub_i32 s33, s24, 0x500
	v_cmp_gt_i32_e64 s[12:13], s33, v176
	s_and_b32 s25, s25, 0x7ffff000
	s_mov_b32 s2, 0xffff0000
	v_readfirstlane_b32 s26, v33
	s_nop 3
	s_cmp_lt_i32 s26, 4
	s_waitcnt vmcnt(5)
	v_cndmask_b32_e32 v4, v29, v4, vcc
	v_cndmask_b32_e64 v134, v3, v2, s[0:1]
	v_cndmask_b32_e32 v134, 0, v134, vcc
	s_waitcnt vmcnt(4)
	v_cndmask_b32_e64 v3, v29, v8, s[4:5]
	v_cndmask_b32_e64 v97, v7, v6, s[0:1]
	v_cndmask_b32_e64 v97, 0, v97, s[4:5]
	v_cndmask_b32_e64 v135, 1.0, v4, s[0:1]
	v_cndmask_b32_e64 v33, -1, v9, s[4:5]
	v_cndmask_b32_e64 v98, 1.0, v3, s[0:1]
	s_waitcnt vmcnt(3)
	v_cndmask_b32_e64 v6, v29, v12, s[6:7]
	v_cndmask_b32_e64 v68, v11, v10, s[0:1]
	v_cndmask_b32_e64 v68, 0, v68, s[6:7]
	s_waitcnt vmcnt(2)
	v_cndmask_b32_e64 v7, v29, v16, s[8:9]
	v_cndmask_b32_e64 v70, 1.0, v6, s[0:1]
	v_cndmask_b32_e64 v73, 1.0, v7, s[0:1]
	v_cndmask_b32_e64 v34, -1, v13, s[6:7]
	v_cndmask_b32_e64 v35, -1, v17, s[8:9]
	v_cndmask_b32_e64 v71, v15, v14, s[0:1]
	v_cndmask_b32_e64 v71, 0, v71, s[8:9]
	s_waitcnt vmcnt(1)
	v_cndmask_b32_e64 v8, v29, v20, s[10:11]
	v_cndmask_b32_e64 v48, 1.0, v8, s[0:1]
	s_waitcnt vmcnt(0)
	v_cndmask_b32_e64 v10, v29, v24, s[12:13]
	v_cndmask_b32_e32 v29, -1, v5, vcc
	v_max_i32_e32 v4, 0, v29
	v_add_u32_e32 v4, s25, v4
	v_mov_b32_e32 v5, 0
	v_lshl_add_u64 v[6:7], v[4:5], 2, s[16:17]
	v_max_i32_e32 v4, 0, v33
	v_add_u32_e32 v4, s25, v4
	v_lshl_add_u64 v[8:9], v[4:5], 2, s[16:17]
	v_max_i32_e32 v4, 0, v34
	v_add_u32_e32 v4, s25, v4
	v_cndmask_b32_e64 v3, 1.0, v10, s[0:1]
	v_lshl_add_u64 v[10:11], v[4:5], 2, s[16:17]
	v_max_i32_e32 v4, 0, v35
	v_cndmask_b32_e64 v36, -1, v21, s[10:11]
	v_add_u32_e32 v4, s25, v4
	v_lshl_add_u64 v[12:13], v[4:5], 2, s[16:17]
	v_max_i32_e32 v4, 0, v36
	v_cndmask_b32_e64 v37, -1, v25, s[12:13]
	v_add_u32_e32 v4, s25, v4
	v_lshl_add_u64 v[14:15], v[4:5], 2, s[16:17]
	v_max_i32_e32 v4, 0, v37
	v_cndmask_b32_e64 v46, v19, v18, s[0:1]
	v_cndmask_b32_e64 v46, 0, v46, s[10:11]
	v_cndmask_b32_e64 v2, v23, v22, s[0:1]
	v_cndmask_b32_e64 v2, 0, v2, s[12:13]
	v_add_u32_e32 v4, s25, v4
	v_lshl_add_u64 v[4:5], v[4:5], 2, s[16:17]
	s_cmpk_lt_i32 s24, 0x801
	s_cselect_b32 s47, 1, 0
	s_cbranch_scc0 .Lffc_nocache
	s_lshl_b32 s46, s27, 12
	s_add_u32 s46, s46, 0x8000
	s_add_u32 s44, s20, s46
	s_addc_u32 s45, s21, 0
	v_lshlrev_b32_e32 v183, 4, v38
	global_load_dwordx4 v[184:187], v183, s[44:45]
	global_load_dwordx4 v[188:191], v183, s[44:45] offset:1024
	global_load_dwordx4 v[192:195], v183, s[44:45] offset:2048
	global_load_dwordx4 v[196:199], v183, s[44:45] offset:3072
.Lffc_nocache:
	s_cmp_lt_i32 s26, 4
	global_load_dword v133, v[6:7], off
	global_load_dword v132, v[8:9], off
	global_load_dword v131, v[10:11], off
	global_load_dword v130, v[12:13], off
	global_load_dword v129, v[14:15], off
	global_load_dword v128, v[4:5], off
	v_max_f32_e32 v6, v32, v32
	v_cndmask_b32_e64 v4, v31, v30, s[0:1]
	v_max_f32_e32 v6, 0xc6ea6000, v6
	v_cndmask_b32_e64 v6, v6, 1.0, s[0:1]
	v_and_b32_e32 v7, 0xffff0000, v4
	v_sub_f32_e32 v8, v4, v7
	v_or_b32_sdwa v22, v4, v7 dst_sel:DWORD dst_unused:UNUSED_PAD src0_sel:WORD_1 src1_sel:DWORD
	v_and_b32_e32 v4, 0xffff0000, v6
	v_sub_f32_e32 v7, v6, v4
	v_or_b32_sdwa v24, v6, v4 dst_sel:DWORD dst_unused:UNUSED_PAD src0_sel:WORD_1 src1_sel:DWORD
	v_or_b32_sdwa v23, v8, v4 dst_sel:DWORD dst_unused:UNUSED_PAD src0_sel:WORD_1 src1_sel:DWORD
	v_max_f32_e32 v4, v28, v28
	v_cndmask_b32_e64 v5, v27, v26, s[0:1]
	v_and_b32_e32 v9, 0xffff0000, v7
	v_max_f32_e32 v4, 0xc6ea6000, v4
	v_sub_f32_e32 v9, v7, v9
	v_lshrrev_b32_e32 v7, 16, v7
	v_cndmask_b32_e64 v4, v4, 1.0, s[0:1]
	v_and_b32_e32 v6, 0xffff0000, v5
	v_and_or_b32 v25, v9, s2, v7
	v_sub_f32_e32 v7, v5, v6
	v_or_b32_sdwa v18, v5, v6 dst_sel:DWORD dst_unused:UNUSED_PAD src0_sel:WORD_1 src1_sel:DWORD
	v_and_b32_e32 v5, 0xffff0000, v4
	v_sub_f32_e32 v6, v4, v5
	v_and_b32_e32 v8, 0xffff0000, v6
	v_sub_f32_e32 v8, v6, v8
	v_lshrrev_b32_e32 v6, 16, v6
	v_or_b32_sdwa v20, v4, v5 dst_sel:DWORD dst_unused:UNUSED_PAD src0_sel:WORD_1 src1_sel:DWORD
	v_or_b32_sdwa v19, v7, v5 dst_sel:DWORD dst_unused:UNUSED_PAD src0_sel:WORD_1 src1_sel:DWORD
	v_and_or_b32 v21, v8, s2, v6
	s_mov_b64 s[2:3], 0
	s_cbranch_scc1 .LBB3_11
	s_cmp_gt_i32 s26, 4
	s_cbranch_scc0 .LBB3_14
	s_cmp_gt_i32 s26, 5
	s_cbranch_scc0 .LBB3_15
	s_cmp_eq_u32 s26, 6
	s_mov_b64 s[4:5], 0
	s_cbranch_scc0 .LBB3_48
	v_and_b32_e32 v4, 0xffff0000, v2
	v_max_f32_e32 v3, v3, v3
	v_sub_f32_e32 v4, v2, v4
	v_max_f32_e32 v3, 0xc6ea6000, v3
	v_and_b32_e32 v5, 0xffff0000, v3
	v_and_b32_e32 v4, 0xffff0000, v4
	v_or_b32_sdwa v75, v5, v2 dst_sel:DWORD dst_unused:UNUSED_PAD src0_sel:DWORD src1_sel:WORD_1
	v_or_b32_sdwa v74, v4, v2 dst_sel:DWORD dst_unused:UNUSED_PAD src0_sel:DWORD src1_sel:WORD_1
	v_sub_f32_e32 v2, v3, v5
	v_and_b32_e32 v4, 0xffff0000, v2
	s_mov_b32 s6, 0xffff0000
	v_sub_f32_e32 v4, v2, v4
	v_lshrrev_b32_e32 v2, 16, v2
	v_and_or_b32 v76, v4, s6, v2
	v_or_b32_sdwa v77, v3, v5 dst_sel:DWORD dst_unused:UNUSED_PAD src0_sel:WORD_1 src1_sel:DWORD
	s_movk_i32 s6, 0xfc00
	s_mov_b64 s[8:9], -1
	v_mfma_f32_32x32x16_bf16 v[2:17], v[22:25], v[74:77], 0
	s_nop 11
	v_cvt_pk_f16_f32 v2, v2, v3
	v_cvt_pk_f16_f32 v3, v4, v5
	v_pk_max_i16 v2, v2, s6 op_sel_hi:[1,0]
	v_pk_max_i16 v3, v3, s6 op_sel_hi:[1,0]
	s_nop 0
	v_exp_f16_e32 v43, v2
	v_exp_f16_e32 v45, v3
	v_exp_f16_sdwa v43, v2 dst_sel:WORD_1 dst_unused:UNUSED_PRESERVE src0_sel:WORD_1
	v_exp_f16_sdwa v45, v3 dst_sel:WORD_1 dst_unused:UNUSED_PRESERVE src0_sel:WORD_1
	v_cvt_pk_f16_f32 v2, v6, v7
	v_cvt_pk_f16_f32 v3, v8, v9
	v_pk_max_i16 v2, v2, s6 op_sel_hi:[1,0]
	v_pk_max_i16 v3, v3, s6 op_sel_hi:[1,0]
	s_nop 0
	v_exp_f16_e32 v50, v2
	v_exp_f16_e32 v54, v3
	v_exp_f16_sdwa v50, v2 dst_sel:WORD_1 dst_unused:UNUSED_PRESERVE src0_sel:WORD_1
	v_exp_f16_sdwa v54, v3 dst_sel:WORD_1 dst_unused:UNUSED_PRESERVE src0_sel:WORD_1
	v_cvt_pk_f16_f32 v2, v10, v11
	v_cvt_pk_f16_f32 v3, v12, v13
	v_pk_max_i16 v2, v2, s6 op_sel_hi:[1,0]
	v_pk_max_i16 v3, v3, s6 op_sel_hi:[1,0]
	s_nop 0
	v_exp_f16_e32 v58, v2
	v_exp_f16_e32 v61, v3
	v_exp_f16_sdwa v58, v2 dst_sel:WORD_1 dst_unused:UNUSED_PRESERVE src0_sel:WORD_1
	v_exp_f16_sdwa v61, v3 dst_sel:WORD_1 dst_unused:UNUSED_PRESERVE src0_sel:WORD_1
	v_cvt_pk_f16_f32 v2, v14, v15
	v_cvt_pk_f16_f32 v3, v16, v17
	v_pk_max_i16 v2, v2, s6 op_sel_hi:[1,0]
	v_pk_max_i16 v3, v3, s6 op_sel_hi:[1,0]
	s_nop 0
	v_exp_f16_e32 v64, v2
	v_exp_f16_e32 v66, v3
	v_exp_f16_sdwa v64, v2 dst_sel:WORD_1 dst_unused:UNUSED_PRESERVE src0_sel:WORD_1
	v_exp_f16_sdwa v66, v3 dst_sel:WORD_1 dst_unused:UNUSED_PRESERVE src0_sel:WORD_1
	v_mfma_f32_32x32x16_bf16 v[2:17], v[18:21], v[74:77], 0
	s_nop 11
	v_cvt_pk_f16_f32 v2, v2, v3
	v_cvt_pk_f16_f32 v3, v4, v5
	v_pk_max_i16 v2, v2, s6 op_sel_hi:[1,0]
	v_pk_max_i16 v3, v3, s6 op_sel_hi:[1,0]
	s_nop 0
	v_exp_f16_e32 v72, v2
	v_exp_f16_e32 v76, v3
	v_exp_f16_sdwa v72, v2 dst_sel:WORD_1 dst_unused:UNUSED_PRESERVE src0_sel:WORD_1
	v_exp_f16_sdwa v76, v3 dst_sel:WORD_1 dst_unused:UNUSED_PRESERVE src0_sel:WORD_1
	v_cvt_pk_f16_f32 v2, v6, v7
	v_cvt_pk_f16_f32 v3, v8, v9
	v_pk_max_i16 v2, v2, s6 op_sel_hi:[1,0]
	v_pk_max_i16 v3, v3, s6 op_sel_hi:[1,0]
	s_nop 0
	v_exp_f16_e32 v83, v2
	v_exp_f16_e32 v85, v3
	v_exp_f16_sdwa v83, v2 dst_sel:WORD_1 dst_unused:UNUSED_PRESERVE src0_sel:WORD_1
	v_exp_f16_sdwa v85, v3 dst_sel:WORD_1 dst_unused:UNUSED_PRESERVE src0_sel:WORD_1
	v_cvt_pk_f16_f32 v2, v10, v11
	v_cvt_pk_f16_f32 v3, v12, v13
	v_pk_max_i16 v2, v2, s6 op_sel_hi:[1,0]
	v_pk_max_i16 v3, v3, s6 op_sel_hi:[1,0]
	s_nop 0
	v_exp_f16_e32 v89, v2
	v_exp_f16_e32 v92, v3
	v_exp_f16_sdwa v89, v2 dst_sel:WORD_1 dst_unused:UNUSED_PRESERVE src0_sel:WORD_1
	v_exp_f16_sdwa v92, v3 dst_sel:WORD_1 dst_unused:UNUSED_PRESERVE src0_sel:WORD_1
	v_cvt_pk_f16_f32 v2, v14, v15
	v_cvt_pk_f16_f32 v3, v16, v17
	v_pk_max_i16 v2, v2, s6 op_sel_hi:[1,0]
	v_pk_max_i16 v3, v3, s6 op_sel_hi:[1,0]
	s_nop 0
	v_exp_f16_e32 v95, v2
	v_exp_f16_e32 v96, v3
	v_exp_f16_sdwa v95, v2 dst_sel:WORD_1 dst_unused:UNUSED_PRESERVE src0_sel:WORD_1
	v_exp_f16_sdwa v96, v3 dst_sel:WORD_1 dst_unused:UNUSED_PRESERVE src0_sel:WORD_1
	s_and_b64 vcc, exec, s[4:5]
	s_cbranch_vccnz .LBB3_16
	s_branch .LBB3_17

.LBB3_36:
.LBB3_37:
	s_and_b64 vcc, exec, s[4:5]
	s_cbranch_vccz .LBB3_39
	s_cmp_eq_u32 s47, 0
	s_cbranch_scc1 .Lffc_nb0_compute
	s_waitcnt vmcnt(6)
	v_mov_b32_e32 v117, v184
	v_mov_b32_e32 v113, v185
	v_mov_b32_e32 v118, v186
	v_mov_b32_e32 v114, v187
	v_mov_b32_e32 v120, v188
	v_mov_b32_e32 v115, v189
	v_mov_b32_e32 v122, v190
	v_mov_b32_e32 v116, v191
	v_mov_b32_e32 v124, v192
	v_mov_b32_e32 v119, v193
	v_mov_b32_e32 v125, v194
	v_mov_b32_e32 v121, v195
	v_mov_b32_e32 v126, v196
	v_mov_b32_e32 v123, v197
	v_mov_b32_e32 v127, v198
	v_mov_b32_e32 v17, v199
	s_branch .LBB3_39
.Lffc_nb0_compute:
	v_max_f32_e32 v2, v135, v135
	v_max_f32_e32 v2, 0xc6ea6000, v2
	v_and_b32_e32 v4, 0xffff0000, v2
	v_and_b32_e32 v3, 0xffff0000, v134
	v_sub_f32_e32 v5, v2, v4
	v_sub_f32_e32 v3, v134, v3
	v_and_b32_e32 v6, 0xffff0000, v5
	s_mov_b32 s2, 0xffff0000
	v_and_b32_e32 v3, 0xffff0000, v3
	v_sub_f32_e32 v6, v5, v6
	v_lshrrev_b32_e32 v5, 16, v5
	v_or_b32_sdwa v125, v4, v134 dst_sel:DWORD dst_unused:UNUSED_PAD src0_sel:DWORD src1_sel:WORD_1
	v_or_b32_sdwa v124, v3, v134 dst_sel:DWORD dst_unused:UNUSED_PAD src0_sel:DWORD src1_sel:WORD_1
	v_and_or_b32 v126, v6, s2, v5
	v_or_b32_sdwa v127, v2, v4 dst_sel:DWORD dst_unused:UNUSED_PAD src0_sel:WORD_1 src1_sel:DWORD
	s_movk_i32 s2, 0xfc00
	s_nop 0
	v_mfma_f32_32x32x16_bf16 v[2:17], v[22:25], v[124:127], 0
	s_nop 11
	v_cvt_pk_f16_f32 v2, v2, v3
	v_cvt_pk_f16_f32 v3, v4, v5
	v_pk_max_i16 v2, v2, s2 op_sel_hi:[1,0]
	v_pk_max_i16 v3, v3, s2 op_sel_hi:[1,0]
	s_nop 0
	v_exp_f16_e32 v117, v2
	v_exp_f16_e32 v113, v3
	v_exp_f16_sdwa v117, v2 dst_sel:WORD_1 dst_unused:UNUSED_PRESERVE src0_sel:WORD_1
	v_exp_f16_sdwa v113, v3 dst_sel:WORD_1 dst_unused:UNUSED_PRESERVE src0_sel:WORD_1
	v_cvt_pk_f16_f32 v2, v6, v7
	v_cvt_pk_f16_f32 v3, v8, v9
	v_pk_max_i16 v2, v2, s2 op_sel_hi:[1,0]
	v_pk_max_i16 v3, v3, s2 op_sel_hi:[1,0]
	s_nop 0
	v_exp_f16_e32 v118, v2
	v_exp_f16_e32 v114, v3
	v_exp_f16_sdwa v118, v2 dst_sel:WORD_1 dst_unused:UNUSED_PRESERVE src0_sel:WORD_1
	v_exp_f16_sdwa v114, v3 dst_sel:WORD_1 dst_unused:UNUSED_PRESERVE src0_sel:WORD_1
	v_cvt_pk_f16_f32 v2, v10, v11
	v_cvt_pk_f16_f32 v3, v12, v13
	v_pk_max_i16 v2, v2, s2 op_sel_hi:[1,0]
	v_pk_max_i16 v3, v3, s2 op_sel_hi:[1,0]
	s_nop 0
	v_exp_f16_e32 v120, v2
	v_exp_f16_e32 v115, v3
	v_exp_f16_sdwa v120, v2 dst_sel:WORD_1 dst_unused:UNUSED_PRESERVE src0_sel:WORD_1
	v_exp_f16_sdwa v115, v3 dst_sel:WORD_1 dst_unused:UNUSED_PRESERVE src0_sel:WORD_1
	v_cvt_pk_f16_f32 v2, v14, v15
	v_cvt_pk_f16_f32 v3, v16, v17
	v_pk_max_i16 v2, v2, s2 op_sel_hi:[1,0]
	v_pk_max_i16 v3, v3, s2 op_sel_hi:[1,0]
	s_nop 0
	v_exp_f16_e32 v122, v2
	v_exp_f16_e32 v116, v3
	v_exp_f16_sdwa v122, v2 dst_sel:WORD_1 dst_unused:UNUSED_PRESERVE src0_sel:WORD_1
	v_exp_f16_sdwa v116, v3 dst_sel:WORD_1 dst_unused:UNUSED_PRESERVE src0_sel:WORD_1
	v_mfma_f32_32x32x16_bf16 v[2:17], v[18:21], v[124:127], 0
	s_nop 11
	v_cvt_pk_f16_f32 v2, v2, v3
	v_cvt_pk_f16_f32 v3, v4, v5
	v_pk_max_i16 v2, v2, s2 op_sel_hi:[1,0]
	v_pk_max_i16 v3, v3, s2 op_sel_hi:[1,0]
	s_nop 0
	v_exp_f16_e32 v124, v2
	v_exp_f16_e32 v119, v3
	v_exp_f16_sdwa v124, v2 dst_sel:WORD_1 dst_unused:UNUSED_PRESERVE src0_sel:WORD_1
	v_exp_f16_sdwa v119, v3 dst_sel:WORD_1 dst_unused:UNUSED_PRESERVE src0_sel:WORD_1
	v_cvt_pk_f16_f32 v2, v6, v7
	v_cvt_pk_f16_f32 v3, v8, v9
	v_pk_max_i16 v2, v2, s2 op_sel_hi:[1,0]
	v_pk_max_i16 v3, v3, s2 op_sel_hi:[1,0]
	s_nop 0
	v_exp_f16_e32 v125, v2
	v_exp_f16_e32 v121, v3
	v_exp_f16_sdwa v125, v2 dst_sel:WORD_1 dst_unused:UNUSED_PRESERVE src0_sel:WORD_1
	v_exp_f16_sdwa v121, v3 dst_sel:WORD_1 dst_unused:UNUSED_PRESERVE src0_sel:WORD_1
	v_cvt_pk_f16_f32 v2, v10, v11
	v_cvt_pk_f16_f32 v3, v12, v13
	v_pk_max_i16 v2, v2, s2 op_sel_hi:[1,0]
	v_pk_max_i16 v3, v3, s2 op_sel_hi:[1,0]
	s_nop 0
	v_exp_f16_e32 v126, v2
	v_exp_f16_e32 v123, v3
	v_exp_f16_sdwa v126, v2 dst_sel:WORD_1 dst_unused:UNUSED_PRESERVE src0_sel:WORD_1
	v_exp_f16_sdwa v123, v3 dst_sel:WORD_1 dst_unused:UNUSED_PRESERVE src0_sel:WORD_1
	v_cvt_pk_f16_f32 v2, v14, v15
	v_cvt_pk_f16_f32 v3, v16, v17
	v_pk_max_i16 v2, v2, s2 op_sel_hi:[1,0]
	v_pk_max_i16 v3, v3, s2 op_sel_hi:[1,0]
	s_nop 0
	v_exp_f16_e32 v127, v2
	v_exp_f16_e32 v17, v3
	v_exp_f16_sdwa v127, v2 dst_sel:WORD_1 dst_unused:UNUSED_PRESERVE src0_sel:WORD_1
	v_exp_f16_sdwa v17, v3 dst_sel:WORD_1 dst_unused:UNUSED_PRESERVE src0_sel:WORD_1

	.amdhsa_kernel _Z6k_iterILb0ELb0EEvPKfS1_PKiPK15HIP_vector_typeIfLj4EES7_S1_S1_S3_S1_PfS8_S1_S3_PDF16_PS5_SA_PiSA_SB_
		.amdhsa_group_segment_fixed_size 5808
		.amdhsa_private_segment_fixed_size 0
		.amdhsa_kernarg_size 152
		.amdhsa_user_sgpr_count 2
		.amdhsa_user_sgpr_dispatch_ptr 0
		.amdhsa_user_sgpr_queue_ptr 0
		.amdhsa_user_sgpr_kernarg_segment_ptr 1
		.amdhsa_user_sgpr_dispatch_id 0
		.amdhsa_user_sgpr_kernarg_preload_length 0
		.amdhsa_user_sgpr_kernarg_preload_offset 0
		.amdhsa_user_sgpr_private_segment_size 0
		.amdhsa_uses_dynamic_stack 0
		.amdhsa_enable_private_segment 0
		.amdhsa_system_sgpr_workgroup_id_x 1
		.amdhsa_system_sgpr_workgroup_id_y 0
		.amdhsa_system_sgpr_workgroup_id_z 0
		.amdhsa_system_sgpr_workgroup_info 0
		.amdhsa_system_vgpr_workitem_id 0
		.amdhsa_next_free_vgpr 200
		.amdhsa_next_free_sgpr 48
		.amdhsa_accum_offset 200
		.amdhsa_reserve_vcc 1
		.amdhsa_float_round_mode_32 0
		.amdhsa_float_round_mode_16_64 0
		.amdhsa_float_denorm_mode_32 3
		.amdhsa_float_denorm_mode_16_64 3
		.amdhsa_dx10_clamp 1
		.amdhsa_ieee_mode 1
		.amdhsa_fp16_overflow 0
		.amdhsa_tg_split 0
		.amdhsa_exception_fp_ieee_invalid_op 0
		.amdhsa_exception_fp_denorm_src 0
		.amdhsa_exception_fp_ieee_div_zero 0
		.amdhsa_exception_fp_ieee_overflow 0
		.amdhsa_exception_fp_ieee_underflow 0
		.amdhsa_exception_fp_ieee_inexact 0
		.amdhsa_exception_int_div_zero 0
	.end_amdhsa_kernel

.LBB4_6:
	s_xor_b32 s33, s32, 0xff
	s_add_i32 s33, s33, s26
	s_ashr_i32 s27, s33, 8
	v_cmp_gt_i32_e32 vcc, s26, v176
	v_med3_i32 v33, s27, 0, 6
	s_sub_i32 s33, s26, 0x100
	v_cmp_gt_i32_e64 s[4:5], s33, v176
	s_sub_i32 s33, s26, 0x200
	v_cmp_gt_i32_e64 s[6:7], s33, v176
	s_sub_i32 s33, s26, 0x300
	v_cmp_gt_i32_e64 s[8:9], s33, v176
	s_sub_i32 s33, s26, 0x400
	v_cmp_gt_i32_e64 s[10:11], s33, v176
	s_sub_i32 s33, s26, 0x500
	v_cmp_gt_i32_e64 s[12:13], s33, v176
	s_and_b32 s27, s29, 0x7ffff000
	s_mov_b32 s2, 0xffff0000
	v_readfirstlane_b32 s28, v33
	s_nop 3
	s_cmp_lt_i32 s28, 4
	s_waitcnt vmcnt(5)
	v_cndmask_b32_e32 v4, v29, v4, vcc
	v_cndmask_b32_e64 v134, v3, v2, s[0:1]
	v_cndmask_b32_e32 v134, 0, v134, vcc
	s_waitcnt vmcnt(4)
	v_cndmask_b32_e64 v3, v29, v8, s[4:5]
	v_cndmask_b32_e64 v97, v7, v6, s[0:1]
	v_cndmask_b32_e64 v97, 0, v97, s[4:5]
	v_cndmask_b32_e64 v135, 1.0, v4, s[0:1]
	v_cndmask_b32_e64 v33, -1, v9, s[4:5]
	v_cndmask_b32_e64 v98, 1.0, v3, s[0:1]
	s_waitcnt vmcnt(3)
	v_cndmask_b32_e64 v6, v29, v12, s[6:7]
	v_cndmask_b32_e64 v68, v11, v10, s[0:1]
	v_cndmask_b32_e64 v68, 0, v68, s[6:7]
	s_waitcnt vmcnt(2)
	v_cndmask_b32_e64 v7, v29, v16, s[8:9]
	v_cndmask_b32_e64 v70, 1.0, v6, s[0:1]
	v_cndmask_b32_e64 v73, 1.0, v7, s[0:1]
	v_cndmask_b32_e64 v34, -1, v13, s[6:7]
	v_cndmask_b32_e64 v35, -1, v17, s[8:9]
	v_cndmask_b32_e64 v71, v15, v14, s[0:1]
	v_cndmask_b32_e64 v71, 0, v71, s[8:9]
	s_waitcnt vmcnt(1)
	v_cndmask_b32_e64 v8, v29, v20, s[10:11]
	v_cndmask_b32_e64 v48, 1.0, v8, s[0:1]
	s_waitcnt vmcnt(0)
	v_cndmask_b32_e64 v10, v29, v24, s[12:13]
	v_cndmask_b32_e32 v29, -1, v5, vcc
	v_max_i32_e32 v4, 0, v29
	v_add_u32_e32 v4, s27, v4
	v_mov_b32_e32 v5, 0
	v_lshl_add_u64 v[6:7], v[4:5], 2, s[16:17]
	v_max_i32_e32 v4, 0, v33
	v_add_u32_e32 v4, s27, v4
	v_lshl_add_u64 v[8:9], v[4:5], 2, s[16:17]
	v_max_i32_e32 v4, 0, v34
	v_add_u32_e32 v4, s27, v4
	v_cndmask_b32_e64 v3, 1.0, v10, s[0:1]
	v_lshl_add_u64 v[10:11], v[4:5], 2, s[16:17]
	v_max_i32_e32 v4, 0, v35
	v_cndmask_b32_e64 v36, -1, v21, s[10:11]
	v_add_u32_e32 v4, s27, v4
	v_lshl_add_u64 v[12:13], v[4:5], 2, s[16:17]
	v_max_i32_e32 v4, 0, v36
	v_cndmask_b32_e64 v37, -1, v25, s[12:13]
	v_add_u32_e32 v4, s27, v4
	v_lshl_add_u64 v[14:15], v[4:5], 2, s[16:17]
	v_max_i32_e32 v4, 0, v37
	v_cndmask_b32_e64 v46, v19, v18, s[0:1]
	v_cndmask_b32_e64 v46, 0, v46, s[10:11]
	v_cndmask_b32_e64 v2, v23, v22, s[0:1]
	v_cndmask_b32_e64 v2, 0, v2, s[12:13]
	v_add_u32_e32 v4, s27, v4
	v_lshl_add_u64 v[4:5], v[4:5], 2, s[16:17]
	s_cmpk_lt_i32 s26, 0x801
	s_cselect_b32 s47, 1, 0
	s_cbranch_scc0 .Lftc_nocache
	s_lshl_b32 s46, s30, 12
	s_add_u32 s46, s46, 0x8000
	s_add_u32 s44, s20, s46
	s_addc_u32 s45, s21, 0
	v_lshlrev_b32_e32 v183, 4, v38
	global_load_dwordx4 v[184:187], v183, s[44:45]
	global_load_dwordx4 v[188:191], v183, s[44:45] offset:1024
	global_load_dwordx4 v[192:195], v183, s[44:45] offset:2048
	global_load_dwordx4 v[196:199], v183, s[44:45] offset:3072
.Lftc_nocache:
	s_cmp_lt_i32 s28, 4
	global_load_dword v133, v[6:7], off
	global_load_dword v132, v[8:9], off
	global_load_dword v131, v[10:11], off
	global_load_dword v130, v[12:13], off
	global_load_dword v129, v[14:15], off
	global_load_dword v128, v[4:5], off
	v_max_f32_e32 v6, v32, v32
	v_cndmask_b32_e64 v4, v31, v30, s[0:1]
	v_max_f32_e32 v6, 0xc6ea6000, v6
	v_cndmask_b32_e64 v6, v6, 1.0, s[0:1]
	v_and_b32_e32 v7, 0xffff0000, v4
	v_sub_f32_e32 v8, v4, v7
	v_or_b32_sdwa v22, v4, v7 dst_sel:DWORD dst_unused:UNUSED_PAD src0_sel:WORD_1 src1_sel:DWORD
	v_and_b32_e32 v4, 0xffff0000, v6
	v_sub_f32_e32 v7, v6, v4
	v_or_b32_sdwa v24, v6, v4 dst_sel:DWORD dst_unused:UNUSED_PAD src0_sel:WORD_1 src1_sel:DWORD
	v_or_b32_sdwa v23, v8, v4 dst_sel:DWORD dst_unused:UNUSED_PAD src0_sel:WORD_1 src1_sel:DWORD
	v_max_f32_e32 v4, v28, v28
	v_cndmask_b32_e64 v5, v27, v26, s[0:1]
	v_and_b32_e32 v9, 0xffff0000, v7
	v_max_f32_e32 v4, 0xc6ea6000, v4
	v_sub_f32_e32 v9, v7, v9
	v_lshrrev_b32_e32 v7, 16, v7
	v_cndmask_b32_e64 v4, v4, 1.0, s[0:1]
	v_and_b32_e32 v6, 0xffff0000, v5
	v_and_or_b32 v25, v9, s2, v7
	v_sub_f32_e32 v7, v5, v6
	v_or_b32_sdwa v18, v5, v6 dst_sel:DWORD dst_unused:UNUSED_PAD src0_sel:WORD_1 src1_sel:DWORD
	v_and_b32_e32 v5, 0xffff0000, v4
	v_sub_f32_e32 v6, v4, v5
	v_and_b32_e32 v8, 0xffff0000, v6
	v_sub_f32_e32 v8, v6, v8
	v_lshrrev_b32_e32 v6, 16, v6
	v_or_b32_sdwa v20, v4, v5 dst_sel:DWORD dst_unused:UNUSED_PAD src0_sel:WORD_1 src1_sel:DWORD
	v_or_b32_sdwa v19, v7, v5 dst_sel:DWORD dst_unused:UNUSED_PAD src0_sel:WORD_1 src1_sel:DWORD
	v_and_or_b32 v21, v8, s2, v6
	s_mov_b64 s[2:3], 0
	s_cbranch_scc1 .LBB4_11
	s_cmp_gt_i32 s28, 4
	s_cbranch_scc0 .LBB4_14
	s_cmp_gt_i32 s28, 5
	s_cbranch_scc0 .LBB4_15
	s_cmp_eq_u32 s28, 6
	s_mov_b64 s[4:5], 0
	s_cbranch_scc0 .LBB4_48
	v_and_b32_e32 v4, 0xffff0000, v2
	v_max_f32_e32 v3, v3, v3
	v_sub_f32_e32 v4, v2, v4
	v_max_f32_e32 v3, 0xc6ea6000, v3
	v_and_b32_e32 v5, 0xffff0000, v3
	v_and_b32_e32 v4, 0xffff0000, v4
	v_or_b32_sdwa v75, v5, v2 dst_sel:DWORD dst_unused:UNUSED_PAD src0_sel:DWORD src1_sel:WORD_1
	v_or_b32_sdwa v74, v4, v2 dst_sel:DWORD dst_unused:UNUSED_PAD src0_sel:DWORD src1_sel:WORD_1
	v_sub_f32_e32 v2, v3, v5
	v_and_b32_e32 v4, 0xffff0000, v2
	s_mov_b32 s6, 0xffff0000
	v_sub_f32_e32 v4, v2, v4
	v_lshrrev_b32_e32 v2, 16, v2
	v_and_or_b32 v76, v4, s6, v2
	v_or_b32_sdwa v77, v3, v5 dst_sel:DWORD dst_unused:UNUSED_PAD src0_sel:WORD_1 src1_sel:DWORD
	s_movk_i32 s6, 0xfc00
	s_mov_b64 s[8:9], -1
	v_mfma_f32_32x32x16_bf16 v[2:17], v[22:25], v[74:77], 0
	s_nop 11
	v_cvt_pk_f16_f32 v2, v2, v3
	v_cvt_pk_f16_f32 v3, v4, v5
	v_pk_max_i16 v2, v2, s6 op_sel_hi:[1,0]
	v_pk_max_i16 v3, v3, s6 op_sel_hi:[1,0]
	s_nop 0
	v_exp_f16_e32 v43, v2
	v_exp_f16_e32 v45, v3
	v_exp_f16_sdwa v43, v2 dst_sel:WORD_1 dst_unused:UNUSED_PRESERVE src0_sel:WORD_1
	v_exp_f16_sdwa v45, v3 dst_sel:WORD_1 dst_unused:UNUSED_PRESERVE src0_sel:WORD_1
	v_cvt_pk_f16_f32 v2, v6, v7
	v_cvt_pk_f16_f32 v3, v8, v9
	v_pk_max_i16 v2, v2, s6 op_sel_hi:[1,0]
	v_pk_max_i16 v3, v3, s6 op_sel_hi:[1,0]
	s_nop 0
	v_exp_f16_e32 v50, v2
	v_exp_f16_e32 v54, v3
	v_exp_f16_sdwa v50, v2 dst_sel:WORD_1 dst_unused:UNUSED_PRESERVE src0_sel:WORD_1
	v_exp_f16_sdwa v54, v3 dst_sel:WORD_1 dst_unused:UNUSED_PRESERVE src0_sel:WORD_1
	v_cvt_pk_f16_f32 v2, v10, v11
	v_cvt_pk_f16_f32 v3, v12, v13
	v_pk_max_i16 v2, v2, s6 op_sel_hi:[1,0]
	v_pk_max_i16 v3, v3, s6 op_sel_hi:[1,0]
	s_nop 0
	v_exp_f16_e32 v58, v2
	v_exp_f16_e32 v61, v3
	v_exp_f16_sdwa v58, v2 dst_sel:WORD_1 dst_unused:UNUSED_PRESERVE src0_sel:WORD_1
	v_exp_f16_sdwa v61, v3 dst_sel:WORD_1 dst_unused:UNUSED_PRESERVE src0_sel:WORD_1
	v_cvt_pk_f16_f32 v2, v14, v15
	v_cvt_pk_f16_f32 v3, v16, v17
	v_pk_max_i16 v2, v2, s6 op_sel_hi:[1,0]
	v_pk_max_i16 v3, v3, s6 op_sel_hi:[1,0]
	s_nop 0
	v_exp_f16_e32 v64, v2
	v_exp_f16_e32 v66, v3
	v_exp_f16_sdwa v64, v2 dst_sel:WORD_1 dst_unused:UNUSED_PRESERVE src0_sel:WORD_1
	v_exp_f16_sdwa v66, v3 dst_sel:WORD_1 dst_unused:UNUSED_PRESERVE src0_sel:WORD_1
	v_mfma_f32_32x32x16_bf16 v[2:17], v[18:21], v[74:77], 0
	s_nop 11
	v_cvt_pk_f16_f32 v2, v2, v3
	v_cvt_pk_f16_f32 v3, v4, v5
	v_pk_max_i16 v2, v2, s6 op_sel_hi:[1,0]
	v_pk_max_i16 v3, v3, s6 op_sel_hi:[1,0]
	s_nop 0
	v_exp_f16_e32 v72, v2
	v_exp_f16_e32 v76, v3
	v_exp_f16_sdwa v72, v2 dst_sel:WORD_1 dst_unused:UNUSED_PRESERVE src0_sel:WORD_1
	v_exp_f16_sdwa v76, v3 dst_sel:WORD_1 dst_unused:UNUSED_PRESERVE src0_sel:WORD_1
	v_cvt_pk_f16_f32 v2, v6, v7
	v_cvt_pk_f16_f32 v3, v8, v9
	v_pk_max_i16 v2, v2, s6 op_sel_hi:[1,0]
	v_pk_max_i16 v3, v3, s6 op_sel_hi:[1,0]
	s_nop 0
	v_exp_f16_e32 v83, v2
	v_exp_f16_e32 v85, v3
	v_exp_f16_sdwa v83, v2 dst_sel:WORD_1 dst_unused:UNUSED_PRESERVE src0_sel:WORD_1
	v_exp_f16_sdwa v85, v3 dst_sel:WORD_1 dst_unused:UNUSED_PRESERVE src0_sel:WORD_1
	v_cvt_pk_f16_f32 v2, v10, v11
	v_cvt_pk_f16_f32 v3, v12, v13
	v_pk_max_i16 v2, v2, s6 op_sel_hi:[1,0]
	v_pk_max_i16 v3, v3, s6 op_sel_hi:[1,0]
	s_nop 0
	v_exp_f16_e32 v89, v2
	v_exp_f16_e32 v92, v3
	v_exp_f16_sdwa v89, v2 dst_sel:WORD_1 dst_unused:UNUSED_PRESERVE src0_sel:WORD_1
	v_exp_f16_sdwa v92, v3 dst_sel:WORD_1 dst_unused:UNUSED_PRESERVE src0_sel:WORD_1
	v_cvt_pk_f16_f32 v2, v14, v15
	v_cvt_pk_f16_f32 v3, v16, v17
	v_pk_max_i16 v2, v2, s6 op_sel_hi:[1,0]
	v_pk_max_i16 v3, v3, s6 op_sel_hi:[1,0]
	s_nop 0
	v_exp_f16_e32 v95, v2
	v_exp_f16_e32 v96, v3
	v_exp_f16_sdwa v95, v2 dst_sel:WORD_1 dst_unused:UNUSED_PRESERVE src0_sel:WORD_1
	v_exp_f16_sdwa v96, v3 dst_sel:WORD_1 dst_unused:UNUSED_PRESERVE src0_sel:WORD_1
	s_and_b64 vcc, exec, s[4:5]
	s_cbranch_vccnz .LBB4_16
	s_branch .LBB4_17

.LBB4_39:
	s_waitcnt vmcnt(5)
	v_rcp_f32_e32 v2, v133
	s_waitcnt vmcnt(4)
	v_rcp_f32_e32 v3, v132
	s_waitcnt vmcnt(3)
	v_rcp_f32_e32 v4, v131
	v_cmp_lt_f32_e32 vcc, 0, v133
	s_waitcnt vmcnt(2)
	v_rcp_f32_e32 v5, v130
	s_waitcnt vmcnt(1)
	v_rcp_f32_e32 v6, v129
	v_cndmask_b32_e32 v2, 0, v2, vcc
	v_cmp_lt_f32_e32 vcc, 0, v132
	s_waitcnt vmcnt(0)
	v_rcp_f32_e32 v7, v128
	s_getpc_b64 s[36:37]
	s_sub_u32 s36, s36, 0x94d8
	s_subb_u32 s37, s37, 0
	v_lshlrev_b32_e32 v183, 6, v0
	v_min_u32_e32 v183, 0x1d80, v183
	global_load_dword v183, v183, s[36:37]
	v_lshlrev_b32_e32 v182, 6, v38
	global_load_dword v182, v182, s[38:39]
	s_lshl_b32 s40, s29, 10
	s_add_u32 s40, s42, s40
	s_addc_u32 s41, s43, 0
	v_lshlrev_b32_e32 v181, 6, v0
	v_and_b32_e32 v181, 0x7fc0, v181
	global_load_dword v181, v181, s[40:41]
	s_mov_b32 s4, 0x42c80000
	v_cndmask_b32_e32 v3, 0, v3, vcc
	v_cmp_lt_f32_e32 vcc, 0, v131
	v_cmp_ngt_f32_e64 s[2:3], s4, v3
	s_mov_b64 s[6:7], 0
	v_cndmask_b32_e32 v4, 0, v4, vcc
	v_cmp_lt_f32_e32 vcc, 0, v130
	s_nop 1
	v_cndmask_b32_e32 v5, 0, v5, vcc
	v_cmp_lt_f32_e32 vcc, 0, v129
	s_nop 1
	v_cndmask_b32_e32 v6, 0, v6, vcc
	v_cmp_lt_f32_e32 vcc, 0, v128
	s_nop 1
	v_cndmask_b32_e32 v7, 0, v7, vcc
	v_cmp_ngt_f32_e32 vcc, s4, v2
	s_or_b64 s[2:3], vcc, s[2:3]
	v_cmp_ngt_f32_e32 vcc, s4, v4
	s_or_b64 s[2:3], s[2:3], vcc
	v_cmp_ngt_f32_e32 vcc, s4, v5
	s_or_b64 s[2:3], s[2:3], vcc
	v_cmp_ngt_f32_e32 vcc, s4, v6
	s_or_b64 s[2:3], s[2:3], vcc
	v_cmp_ngt_f32_e32 vcc, s4, v7
	s_or_b64 s[2:3], s[2:3], vcc
	v_cndmask_b32_e64 v8, 0, 1, s[2:3]
	v_cmp_ne_u32_e32 vcc, 0, v8
	s_cmp_eq_u64 vcc, 0
	s_cselect_b64 s[2:3], -1, 0
	v_cndmask_b32_e64 v8, 0, 1, s[2:3]
	s_nop 0
	v_readfirstlane_b32 s2, v8
	s_bitcmp0_b32 s2, 0
	s_cbranch_scc0 .LBB4_45
	s_cmp_lt_i32 s28, 4
	s_cbranch_scc1 .LBB4_46
	s_cmp_gt_i32 s28, 4
	s_cbranch_scc0 .LBB4_47
	s_mov_b64 s[4:5], -1
	v_mov_b32_e32 v8, 0
	s_cmp_gt_i32 s28, 5
	v_mov_b32_e32 v167, 0
	v_mov_b32_e32 v166, 0
	v_mov_b32_e32 v165, 0
	v_mov_b32_e32 v164, 0
	v_mov_b32_e32 v162, 0
	v_mov_b32_e32 v160, 0
	v_mov_b32_e32 v159, 0
	v_mov_b32_e32 v157, 0
	v_mov_b32_e32 v151, 0
	v_mov_b32_e32 v149, 0
	v_mov_b32_e32 v147, 0
	v_mov_b32_e32 v146, 0
	v_mov_b32_e32 v144, 0
	v_mov_b32_e32 v143, 0
	v_mov_b32_e32 v152, 0
	v_mov_b32_e32 v153, 0
	v_mov_b32_e32 v154, 0
	v_mov_b32_e32 v155, 0
	v_mov_b32_e32 v156, 0
	v_mov_b32_e32 v158, 0
	v_mov_b32_e32 v161, 0
	v_mov_b32_e32 v163, 0
	v_mov_b32_e32 v168, 0
	v_mov_b32_e32 v169, 0
	v_mov_b32_e32 v170, 0
	v_mov_b32_e32 v171, 0
	v_mov_b32_e32 v172, 0
	v_mov_b32_e32 v173, 0
	v_mov_b32_e32 v174, 0
	v_mov_b32_e32 v145, 0
	v_mov_b32_e32 v148, 0
	v_mov_b32_e32 v150, 0
	s_cbranch_scc0 .LBB4_50
	s_cmp_eq_u32 s28, 6
	s_cbranch_scc0 .LBB4_49
	v_mov_b32_e32 v145, 0
	v_mov_b32_e32 v148, 0
	v_mov_b32_e32 v150, 0
	v_mov_b32_e32 v143, 0
	v_mov_b32_e32 v144, 0
	v_mov_b32_e32 v146, 0
	v_mov_b32_e32 v147, 0
	v_mov_b32_e32 v149, 0
	v_mov_b32_e32 v151, 0
	v_mov_b32_e32 v152, 0
	v_mov_b32_e32 v153, 0
	v_mov_b32_e32 v154, 0
	v_mov_b32_e32 v155, 0
	v_mov_b32_e32 v156, 0
	v_mov_b32_e32 v158, 0
	v_mov_b32_e32 v161, 0
	v_mov_b32_e32 v163, 0
	v_mov_b32_e32 v157, 0
	v_mov_b32_e32 v159, 0
	v_mov_b32_e32 v160, 0
	v_mov_b32_e32 v162, 0
	v_mov_b32_e32 v164, 0
	v_mov_b32_e32 v165, 0
	v_mov_b32_e32 v166, 0
	v_mov_b32_e32 v167, 0
	v_mov_b32_e32 v168, 0
	v_mov_b32_e32 v169, 0
	v_mov_b32_e32 v170, 0
	v_mov_b32_e32 v171, 0
	v_mov_b32_e32 v172, 0
	v_mov_b32_e32 v173, 0
	v_mov_b32_e32 v174, 0
	v_fma_mix_f32 v148, v43, v7, v148 op_sel_hi:[1,0,0]
	v_fma_mix_f32 v150, v45, v7, v150 op_sel_hi:[1,0,0]
	v_fma_mix_f32 v143, v50, v7, v143 op_sel_hi:[1,0,0]
	v_fma_mix_f32 v144, v54, v7, v144 op_sel_hi:[1,0,0]
	v_fma_mix_f32 v146, v58, v7, v146 op_sel_hi:[1,0,0]
	v_fma_mix_f32 v147, v61, v7, v147 op_sel_hi:[1,0,0]
	v_fma_mix_f32 v149, v64, v7, v149 op_sel_hi:[1,0,0]
	v_fma_mix_f32 v151, v66, v7, v151 op_sel_hi:[1,0,0]
	v_fma_mix_f32 v152, v43, v7, v152 op_sel:[1,0,0] op_sel_hi:[1,0,0]
	v_fma_mix_f32 v153, v45, v7, v153 op_sel:[1,0,0] op_sel_hi:[1,0,0]
	v_fma_mix_f32 v154, v50, v7, v154 op_sel:[1,0,0] op_sel_hi:[1,0,0]
	v_fma_mix_f32 v155, v54, v7, v155 op_sel:[1,0,0] op_sel_hi:[1,0,0]
	v_fma_mix_f32 v156, v58, v7, v156 op_sel:[1,0,0] op_sel_hi:[1,0,0]
	v_fma_mix_f32 v158, v61, v7, v158 op_sel:[1,0,0] op_sel_hi:[1,0,0]
	v_fma_mix_f32 v161, v64, v7, v161 op_sel:[1,0,0] op_sel_hi:[1,0,0]
	v_fma_mix_f32 v163, v66, v7, v163 op_sel:[1,0,0] op_sel_hi:[1,0,0]
	v_fma_mix_f32 v157, v72, v7, v157 op_sel_hi:[1,0,0]
	v_fma_mix_f32 v159, v76, v7, v159 op_sel_hi:[1,0,0]
	v_fma_mix_f32 v160, v83, v7, v160 op_sel_hi:[1,0,0]
	v_fma_mix_f32 v162, v85, v7, v162 op_sel_hi:[1,0,0]
	v_fma_mix_f32 v164, v89, v7, v164 op_sel_hi:[1,0,0]
	v_fma_mix_f32 v165, v92, v7, v165 op_sel_hi:[1,0,0]
	v_fma_mix_f32 v166, v95, v7, v166 op_sel_hi:[1,0,0]
	v_fma_mix_f32 v167, v96, v7, v167 op_sel_hi:[1,0,0]
	v_fma_mix_f32 v168, v72, v7, v168 op_sel:[1,0,0] op_sel_hi:[1,0,0]
	v_fma_mix_f32 v169, v76, v7, v169 op_sel:[1,0,0] op_sel_hi:[1,0,0]
	v_fma_mix_f32 v170, v83, v7, v170 op_sel:[1,0,0] op_sel_hi:[1,0,0]
	v_fma_mix_f32 v171, v85, v7, v171 op_sel:[1,0,0] op_sel_hi:[1,0,0]
	v_fma_mix_f32 v172, v89, v7, v172 op_sel:[1,0,0] op_sel_hi:[1,0,0]
	v_fma_mix_f32 v173, v92, v7, v173 op_sel:[1,0,0] op_sel_hi:[1,0,0]
	v_fma_mix_f32 v174, v95, v7, v174 op_sel:[1,0,0] op_sel_hi:[1,0,0]
	v_fma_mix_f32 v145, v96, v7, v145 op_sel:[1,0,0] op_sel_hi:[1,0,0]
	s_branch .LBB4_50

	.amdhsa_kernel _Z6k_iterILb0ELb1EEvPKfS1_PKiPK15HIP_vector_typeIfLj4EES7_S1_S1_S3_S1_PfS8_S1_S3_PDF16_PS5_SA_PiSA_SB_
		.amdhsa_group_segment_fixed_size 5808
		.amdhsa_private_segment_fixed_size 0
		.amdhsa_kernarg_size 152
		.amdhsa_user_sgpr_count 2
		.amdhsa_user_sgpr_dispatch_ptr 0
		.amdhsa_user_sgpr_queue_ptr 0
		.amdhsa_user_sgpr_kernarg_segment_ptr 1
		.amdhsa_user_sgpr_dispatch_id 0
		.amdhsa_user_sgpr_kernarg_preload_length 0
		.amdhsa_user_sgpr_kernarg_preload_offset 0
		.amdhsa_user_sgpr_private_segment_size 0
		.amdhsa_uses_dynamic_stack 0
		.amdhsa_enable_private_segment 0
		.amdhsa_system_sgpr_workgroup_id_x 1
		.amdhsa_system_sgpr_workgroup_id_y 0
		.amdhsa_system_sgpr_workgroup_id_z 0
		.amdhsa_system_sgpr_workgroup_info 0
		.amdhsa_system_vgpr_workitem_id 0
		.amdhsa_next_free_vgpr 200
		.amdhsa_next_free_sgpr 48
		.amdhsa_accum_offset 200
		.amdhsa_reserve_vcc 1
		.amdhsa_float_round_mode_32 0
		.amdhsa_float_round_mode_16_64 0
		.amdhsa_float_denorm_mode_32 3
		.amdhsa_float_denorm_mode_16_64 3
		.amdhsa_dx10_clamp 1
		.amdhsa_ieee_mode 1
		.amdhsa_fp16_overflow 0
		.amdhsa_tg_split 0
		.amdhsa_exception_fp_ieee_invalid_op 0
		.amdhsa_exception_fp_denorm_src 0
		.amdhsa_exception_fp_ieee_div_zero 0
		.amdhsa_exception_fp_ieee_overflow 0
		.amdhsa_exception_fp_ieee_underflow 0
		.amdhsa_exception_fp_ieee_inexact 0
		.amdhsa_exception_int_div_zero 0
	.end_amdhsa_kernel

amdhsa.kernels:
  - .agpr_count:     0
    .args:
      - .actual_access:  read_only
        .address_space:  global
        .offset:         0
        .size:           8
        .value_kind:     global_buffer
      - .actual_access:  read_only
        .address_space:  global
        .offset:         8
        .size:           8
        .value_kind:     global_buffer
      - .actual_access:  read_only
        .address_space:  global
        .offset:         16
        .size:           8
        .value_kind:     global_buffer
      - .actual_access:  read_only
        .address_space:  global
        .offset:         24
        .size:           8
        .value_kind:     global_buffer
      - .actual_access:  write_only
        .address_space:  global
        .offset:         32
        .size:           8
        .value_kind:     global_buffer
      - .actual_access:  write_only
        .address_space:  global
        .offset:         40
        .size:           8
        .value_kind:     global_buffer
      - .actual_access:  write_only
        .address_space:  global
        .offset:         48
        .size:           8
        .value_kind:     global_buffer
      - .actual_access:  write_only
        .address_space:  global
        .offset:         56
        .size:           8
        .value_kind:     global_buffer
      - .actual_access:  write_only
        .address_space:  global
        .offset:         64
        .size:           8
        .value_kind:     global_buffer
      - .actual_access:  write_only
        .address_space:  global
        .offset:         72
        .size:           8
        .value_kind:     global_buffer
      - .actual_access:  write_only
        .address_space:  global
        .offset:         80
        .size:           8
        .value_kind:     global_buffer
      - .actual_access:  write_only
        .address_space:  global
        .offset:         88
        .size:           8
        .value_kind:     global_buffer
      - .actual_access:  write_only
        .address_space:  global
        .offset:         96
        .size:           8
        .value_kind:     global_buffer
      - .actual_access:  write_only
        .address_space:  global
        .offset:         104
        .size:           8
        .value_kind:     global_buffer
      - .actual_access:  write_only
        .address_space:  global
        .offset:         112
        .size:           8
        .value_kind:     global_buffer
    .group_segment_fixed_size: 67584
    .kernarg_segment_align: 8
    .kernarg_segment_size: 120
    .language:       OpenCL C
    .language_version:
      - 2
      - 0
    .max_flat_workgroup_size: 1024
    .name:           _Z6k_sortPKfS0_PKiS2_PiP15HIP_vector_typeIfLj4EEPfS7_S3_S7_S7_S3_S3_S6_S6_
    .private_segment_fixed_size: 0
    .sgpr_count:     58
    .sgpr_spill_count: 0
    .symbol:         _Z6k_sortPKfS0_PKiS2_PiP15HIP_vector_typeIfLj4EEPfS7_S3_S7_S7_S3_S3_S6_S6_.kd
    .uniform_work_group_size: 1
    .uses_dynamic_stack: false
    .vgpr_count:     48
    .vgpr_spill_count: 0
    .wavefront_size: 64
  - .agpr_count:     0
    .args:
      - .actual_access:  read_only
        .address_space:  global
        .offset:         0
        .size:           8
        .value_kind:     global_buffer
      - .actual_access:  read_only
        .address_space:  global
        .offset:         8
        .size:           8
        .value_kind:     global_buffer
      - .actual_access:  read_only
        .address_space:  global
        .offset:         16
        .size:           8
        .value_kind:     global_buffer
      - .actual_access:  read_only
        .address_space:  global
        .offset:         24
        .size:           8
        .value_kind:     global_buffer
      - .actual_access:  read_only
        .address_space:  global
        .offset:         32
        .size:           8
        .value_kind:     global_buffer
      - .actual_access:  read_only
        .address_space:  global
        .offset:         40
        .size:           8
        .value_kind:     global_buffer
      - .actual_access:  read_only
        .address_space:  global
        .offset:         48
        .size:           8
        .value_kind:     global_buffer
      - .actual_access:  write_only
        .address_space:  global
        .offset:         56
        .size:           8
        .value_kind:     global_buffer
    .group_segment_fixed_size: 145952
    .kernarg_segment_align: 8
    .kernarg_segment_size: 64
    .language:       OpenCL C
    .language_version:
      - 2
      - 0
    .max_flat_workgroup_size: 512
    .name:           _Z7k_finalPK15HIP_vector_typeIfLj4EES2_PKiS4_PKfS6_PKDF16_Pf
    .private_segment_fixed_size: 0
    .sgpr_count:     34
    .sgpr_spill_count: 0
    .symbol:         _Z7k_finalPK15HIP_vector_typeIfLj4EES2_PKiS4_PKfS6_PKDF16_Pf.kd
    .uniform_work_group_size: 1
    .uses_dynamic_stack: false
    .vgpr_count:     177
    .vgpr_spill_count: 0
    .wavefront_size: 64
  - .agpr_count:     0
    .args:
      - .actual_access:  read_only
        .address_space:  global
        .offset:         0
        .size:           8
        .value_kind:     global_buffer
      - .actual_access:  read_only
        .address_space:  global
        .offset:         8
        .size:           8
        .value_kind:     global_buffer
      - .actual_access:  read_only
        .address_space:  global
        .offset:         16
        .size:           8
        .value_kind:     global_buffer
      - .actual_access:  read_only
        .address_space:  global
        .offset:         24
        .size:           8
        .value_kind:     global_buffer
      - .actual_access:  read_only
        .address_space:  global
        .offset:         32
        .size:           8
        .value_kind:     global_buffer
      - .actual_access:  read_only
        .address_space:  global
        .offset:         40
        .size:           8
        .value_kind:     global_buffer
      - .actual_access:  read_only
        .address_space:  global
        .offset:         48
        .size:           8
        .value_kind:     global_buffer
      - .actual_access:  read_only
        .address_space:  global
        .offset:         56
        .size:           8
        .value_kind:     global_buffer
      - .actual_access:  read_only
        .address_space:  global
        .offset:         64
        .size:           8
        .value_kind:     global_buffer
      - .address_space:  global
        .offset:         72
        .size:           8
        .value_kind:     global_buffer
      - .actual_access:  read_only
        .address_space:  global
        .offset:         80
        .size:           8
        .value_kind:     global_buffer
      - .actual_access:  read_only
        .address_space:  global
        .offset:         88
        .size:           8
        .value_kind:     global_buffer
      - .actual_access:  read_only
        .address_space:  global
        .offset:         96
        .size:           8
        .value_kind:     global_buffer
      - .actual_access:  write_only
        .address_space:  global
        .offset:         104
        .size:           8
        .value_kind:     global_buffer
      - .address_space:  global
        .offset:         112
        .size:           8
        .value_kind:     global_buffer
      - .actual_access:  write_only
        .address_space:  global
        .offset:         120
        .size:           8
        .value_kind:     global_buffer
      - .actual_access:  write_only
        .address_space:  global
        .offset:         128
        .size:           8
        .value_kind:     global_buffer
      - .actual_access:  write_only
        .address_space:  global
        .offset:         136
        .size:           8
        .value_kind:     global_buffer
      - .actual_access:  write_only
        .address_space:  global
        .offset:         144
        .size:           8
        .value_kind:     global_buffer
    .group_segment_fixed_size: 30384
    .kernarg_segment_align: 8
    .kernarg_segment_size: 152
    .language:       OpenCL C
    .language_version:
      - 2
      - 0
    .max_flat_workgroup_size: 512
    .name:           _Z6k_iterILb1ELb0EEvPKfS1_PKiPK15HIP_vector_typeIfLj4EES7_S1_S1_S3_S1_PfS8_S1_S3_PDF16_PS5_SA_PiSA_SB_
    .private_segment_fixed_size: 0
    .sgpr_count:     108
    .sgpr_spill_count: 0
    .symbol:         _Z6k_iterILb1ELb0EEvPKfS1_PKiPK15HIP_vector_typeIfLj4EES7_S1_S1_S3_S1_PfS8_S1_S3_PDF16_PS5_SA_PiSA_SB_.kd
    .uniform_work_group_size: 1
    .uses_dynamic_stack: false
    .vgpr_count:     256
    .vgpr_spill_count: 0
    .wavefront_size: 64
  - .agpr_count:     0
    .args:
      - .actual_access:  read_only
        .address_space:  global
        .offset:         0
        .size:           8
        .value_kind:     global_buffer
      - .actual_access:  read_only
        .address_space:  global
        .offset:         8
        .size:           8
        .value_kind:     global_buffer
      - .actual_access:  read_only
        .address_space:  global
        .offset:         16
        .size:           8
        .value_kind:     global_buffer
      - .actual_access:  read_only
        .address_space:  global
        .offset:         24
        .size:           8
        .value_kind:     global_buffer
      - .actual_access:  read_only
        .address_space:  global
        .offset:         32
        .size:           8
        .value_kind:     global_buffer
      - .actual_access:  read_only
        .address_space:  global
        .offset:         40
        .size:           8
        .value_kind:     global_buffer
      - .actual_access:  read_only
        .address_space:  global
        .offset:         48
        .size:           8
        .value_kind:     global_buffer
      - .actual_access:  read_only
        .address_space:  global
        .offset:         56
        .size:           8
        .value_kind:     global_buffer
      - .actual_access:  read_only
        .address_space:  global
        .offset:         64
        .size:           8
        .value_kind:     global_buffer
      - .address_space:  global
        .offset:         72
        .size:           8
        .value_kind:     global_buffer
      - .actual_access:  read_only
        .address_space:  global
        .offset:         80
        .size:           8
        .value_kind:     global_buffer
      - .actual_access:  read_only
        .address_space:  global
        .offset:         88
        .size:           8
        .value_kind:     global_buffer
      - .actual_access:  read_only
        .address_space:  global
        .offset:         96
        .size:           8
        .value_kind:     global_buffer
      - .actual_access:  read_only
        .address_space:  global
        .offset:         104
        .size:           8
        .value_kind:     global_buffer
      - .actual_access:  read_only
        .address_space:  global
        .offset:         112
        .size:           8
        .value_kind:     global_buffer
      - .actual_access:  read_only
        .address_space:  global
        .offset:         120
        .size:           8
        .value_kind:     global_buffer
      - .actual_access:  read_only
        .address_space:  global
        .offset:         128
        .size:           8
        .value_kind:     global_buffer
      - .actual_access:  read_only
        .address_space:  global
        .offset:         136
        .size:           8
        .value_kind:     global_buffer
      - .actual_access:  read_only
        .address_space:  global
        .offset:         144
        .size:           8
        .value_kind:     global_buffer
    .group_segment_fixed_size: 5808
    .kernarg_segment_align: 8
    .kernarg_segment_size: 152
    .language:       OpenCL C
    .language_version:
      - 2
      - 0
    .max_flat_workgroup_size: 512
    .name:           _Z6k_iterILb0ELb0EEvPKfS1_PKiPK15HIP_vector_typeIfLj4EES7_S1_S1_S3_S1_PfS8_S1_S3_PDF16_PS5_SA_PiSA_SB_
    .private_segment_fixed_size: 0
    .sgpr_count:     54
    .sgpr_spill_count: 0
    .symbol:         _Z6k_iterILb0ELb0EEvPKfS1_PKiPK15HIP_vector_typeIfLj4EES7_S1_S1_S3_S1_PfS8_S1_S3_PDF16_PS5_SA_PiSA_SB_.kd
    .uniform_work_group_size: 1
    .uses_dynamic_stack: false
    .vgpr_count:     200
    .vgpr_spill_count: 0
    .wavefront_size: 64
  - .agpr_count:     0
    .args:
      - .actual_access:  read_only
        .address_space:  global
        .offset:         0
        .size:           8
        .value_kind:     global_buffer
      - .actual_access:  read_only
        .address_space:  global
        .offset:         8
        .size:           8
        .value_kind:     global_buffer
      - .actual_access:  read_only
        .address_space:  global
        .offset:         16
        .size:           8
        .value_kind:     global_buffer
      - .actual_access:  read_only
        .address_space:  global
        .offset:         24
        .size:           8
        .value_kind:     global_buffer
      - .actual_access:  read_only
        .address_space:  global
        .offset:         32
        .size:           8
        .value_kind:     global_buffer
      - .actual_access:  read_only
        .address_space:  global
        .offset:         40
        .size:           8
        .value_kind:     global_buffer
      - .actual_access:  read_only
        .address_space:  global
        .offset:         48
        .size:           8
        .value_kind:     global_buffer
      - .actual_access:  read_only
        .address_space:  global
        .offset:         56
        .size:           8
        .value_kind:     global_buffer
      - .actual_access:  read_only
        .address_space:  global
        .offset:         64
        .size:           8
        .value_kind:     global_buffer
      - .address_space:  global
        .offset:         72
        .size:           8
        .value_kind:     global_buffer
      - .actual_access:  write_only
        .address_space:  global
        .offset:         80
        .size:           8
        .value_kind:     global_buffer
      - .actual_access:  read_only
        .address_space:  global
        .offset:         88
        .size:           8
        .value_kind:     global_buffer
      - .actual_access:  read_only
        .address_space:  global
        .offset:         96
        .size:           8
        .value_kind:     global_buffer
      - .actual_access:  read_only
        .address_space:  global
        .offset:         104
        .size:           8
        .value_kind:     global_buffer
      - .actual_access:  read_only
        .address_space:  global
        .offset:         112
        .size:           8
        .value_kind:     global_buffer
      - .actual_access:  read_only
        .address_space:  global
        .offset:         120
        .size:           8
        .value_kind:     global_buffer
      - .actual_access:  read_only
        .address_space:  global
        .offset:         128
        .size:           8
        .value_kind:     global_buffer
      - .actual_access:  read_only
        .address_space:  global
        .offset:         136
        .size:           8
        .value_kind:     global_buffer
      - .actual_access:  read_only
        .address_space:  global
        .offset:         144
        .size:           8
        .value_kind:     global_buffer
    .group_segment_fixed_size: 5808
    .kernarg_segment_align: 8
    .kernarg_segment_size: 152
    .language:       OpenCL C
    .language_version:
      - 2
      - 0
    .max_flat_workgroup_size: 512
    .name:           _Z6k_iterILb0ELb1EEvPKfS1_PKiPK15HIP_vector_typeIfLj4EES7_S1_S1_S3_S1_PfS8_S1_S3_PDF16_PS5_SA_PiSA_SB_
    .private_segment_fixed_size: 0
    .sgpr_count:     54
    .sgpr_spill_count: 0
    .symbol:         _Z6k_iterILb0ELb1EEvPKfS1_PKiPK15HIP_vector_typeIfLj4EES7_S1_S1_S3_S1_PfS8_S1_S3_PDF16_PS5_SA_PiSA_SB_.kd
    .uniform_work_group_size: 1
    .uses_dynamic_stack: false
    .vgpr_count:     200
    .vgpr_spill_count: 0
    .wavefront_size: 64
